# baseline (speedup 1.0000x reference)
.LBB1_30:
	s_and_b64 vcc, exec, s[4:5]
	s_cbranch_vccz .LBB1_41
	s_load_dwordx4 s[44:47], s[0:1], 0x0
	s_load_dwordx2 s[48:49], s[0:1], 0x20
	s_mov_b32 s50, s2
	v_and_b32_e32 v1, 31, v0
	v_lshrrev_b32_e32 v2, 5, v0
	v_lshlrev_b32_e32 v3, 5, v1
	v_lshl_add_u32 v3, v2, 13, v3
	v_add_u32_e32 v3, 0x1400, v3
	v_lshlrev_b32_e32 v4, 4, v1
	v_lshl_add_u32 v4, v2, 12, v4
	v_add_u32_e32 v4, 0xa00, v4
	s_waitcnt lgkmcnt(0)
	s_add_u32 s48, s48, 0x408000
	s_addc_u32 s49, s49, 0
	s_load_dwordx4 s[52:55], s[48:49], 0x800
	s_lshl_b32 s51, s50, 18
	s_add_u32 s44, s44, s51
	s_addc_u32 s45, s45, 0
	s_mul_i32 s51, s50, 0x30000
	s_add_u32 s46, s46, s51
	s_addc_u32 s47, s47, 0
	s_waitcnt lgkmcnt(0)
	s_lshl_b32 s51, s50, 19
	s_add_u32 s52, s52, s51
	s_addc_u32 s53, s53, 0
	s_mul_i32 s51, s50, 0x60000
	s_add_u32 s54, s54, s51
	s_addc_u32 s55, s55, 0
	v_cmp_eq_u32_e64 s[78:79], 0, v0
	v_mov_b32_e32 v5, 1
	v_mov_b32_e32 v6, s50
	v_lshlrev_b32_e32 v6, 2, v6
	s_add_u32 s58, s52, 0x0
	s_addc_u32 s59, s53, 0
	global_load_dwordx4 v[16:19], v3, s[58:59] nt
	global_load_dwordx4 v[20:23], v3, s[58:59] offset:16 nt
	s_add_u32 s58, s52, 0x20000
	s_addc_u32 s59, s53, 0
	global_load_dwordx4 v[24:27], v3, s[58:59] nt
	global_load_dwordx4 v[28:31], v3, s[58:59] offset:16 nt
	s_add_u32 s58, s52, 0x40000
	s_addc_u32 s59, s53, 0
	global_load_dwordx4 v[32:35], v3, s[58:59] nt
	global_load_dwordx4 v[36:39], v3, s[58:59] offset:16 nt
	s_add_u32 s58, s52, 0x60000
	s_addc_u32 s59, s53, 0
	global_load_dwordx4 v[40:43], v3, s[58:59] nt
	global_load_dwordx4 v[44:47], v3, s[58:59] offset:16 nt
	s_add_u32 s58, s54, 0x0
	s_addc_u32 s59, s55, 0
	global_load_dwordx4 v[48:51], v3, s[58:59] nt
	global_load_dwordx4 v[52:55], v3, s[58:59] offset:16 nt
	s_add_u32 s58, s54, 0x20000
	s_addc_u32 s59, s55, 0
	global_load_dwordx4 v[56:59], v3, s[58:59] nt
	global_load_dwordx4 v[60:63], v3, s[58:59] offset:16 nt
	s_add_u32 s58, s54, 0x40000
	s_addc_u32 s59, s55, 0
	global_load_dwordx4 v[64:67], v3, s[58:59] nt
	global_load_dwordx4 v[68:71], v3, s[58:59] offset:16 nt
	s_add_u32 s58, s52, 0x400
	s_addc_u32 s59, s53, 0
	global_load_dwordx4 v[72:75], v3, s[58:59] nt
	global_load_dwordx4 v[76:79], v3, s[58:59] offset:16 nt
	s_add_u32 s58, s52, 0x20400
	s_addc_u32 s59, s53, 0
	global_load_dwordx4 v[80:83], v3, s[58:59] nt
	global_load_dwordx4 v[84:87], v3, s[58:59] offset:16 nt
	s_add_u32 s58, s52, 0x40400
	s_addc_u32 s59, s53, 0
	global_load_dwordx4 v[88:91], v3, s[58:59] nt
	global_load_dwordx4 v[92:95], v3, s[58:59] offset:16 nt
	s_add_u32 s58, s52, 0x60400
	s_addc_u32 s59, s53, 0
	global_load_dwordx4 v[96:99], v3, s[58:59] nt
	global_load_dwordx4 v[100:103], v3, s[58:59] offset:16 nt
	s_add_u32 s58, s54, 0x400
	s_addc_u32 s59, s55, 0
	global_load_dwordx4 v[104:107], v3, s[58:59] nt
	global_load_dwordx4 v[108:111], v3, s[58:59] offset:16 nt
	s_add_u32 s58, s54, 0x20400
	s_addc_u32 s59, s55, 0
	global_load_dwordx4 v[112:115], v3, s[58:59] nt
	global_load_dwordx4 v[116:119], v3, s[58:59] offset:16 nt
	s_add_u32 s58, s54, 0x40400
	s_addc_u32 s59, s55, 0
	global_load_dwordx4 v[120:123], v3, s[58:59] nt
	global_load_dwordx4 v[124:127], v3, s[58:59] offset:16 nt
	s_waitcnt vmcnt(26)
	v_cvt_pk_f16_f32 v16, v16, v17
	v_cvt_pk_f16_f32 v17, v18, v19
	v_cvt_pk_f16_f32 v18, v20, v21
	v_cvt_pk_f16_f32 v19, v22, v23
	s_add_u32 s76, s44, 0x0
	s_addc_u32 s77, s45, 0
	global_store_dwordx4 v4, v[16:19], s[76:77] sc1
	s_waitcnt vmcnt(25)
	v_cvt_pk_f16_f32 v24, v24, v25
	v_cvt_pk_f16_f32 v25, v26, v27
	v_cvt_pk_f16_f32 v26, v28, v29
	v_cvt_pk_f16_f32 v27, v30, v31
	s_add_u32 s76, s44, 0x10000
	s_addc_u32 s77, s45, 0
	global_store_dwordx4 v4, v[24:27], s[76:77] sc1
	s_waitcnt vmcnt(24)
	v_cvt_pk_f16_f32 v32, v32, v33
	v_cvt_pk_f16_f32 v33, v34, v35
	v_cvt_pk_f16_f32 v34, v36, v37
	v_cvt_pk_f16_f32 v35, v38, v39
	s_add_u32 s76, s44, 0x20000
	s_addc_u32 s77, s45, 0
	global_store_dwordx4 v4, v[32:35], s[76:77] sc1
	s_waitcnt vmcnt(23)
	v_cvt_pk_f16_f32 v40, v40, v41
	v_cvt_pk_f16_f32 v41, v42, v43
	v_cvt_pk_f16_f32 v42, v44, v45
	v_cvt_pk_f16_f32 v43, v46, v47
	s_add_u32 s76, s44, 0x30000
	s_addc_u32 s77, s45, 0
	global_store_dwordx4 v4, v[40:43], s[76:77] sc1
	s_waitcnt vmcnt(22)
	v_cvt_pk_f16_f32 v48, v48, v49
	v_cvt_pk_f16_f32 v49, v50, v51
	v_cvt_pk_f16_f32 v50, v52, v53
	v_cvt_pk_f16_f32 v51, v54, v55
	s_add_u32 s76, s46, 0x0
	s_addc_u32 s77, s47, 0
	global_store_dwordx4 v4, v[48:51], s[76:77] sc1
	s_waitcnt vmcnt(21)
	v_cvt_pk_f16_f32 v56, v56, v57
	v_cvt_pk_f16_f32 v57, v58, v59
	v_cvt_pk_f16_f32 v58, v60, v61
	v_cvt_pk_f16_f32 v59, v62, v63
	s_add_u32 s76, s46, 0x10000
	s_addc_u32 s77, s47, 0
	global_store_dwordx4 v4, v[56:59], s[76:77] sc1
	s_waitcnt vmcnt(20)
	v_cvt_pk_f16_f32 v64, v64, v65
	v_cvt_pk_f16_f32 v65, v66, v67
	v_cvt_pk_f16_f32 v66, v68, v69
	v_cvt_pk_f16_f32 v67, v70, v71
	s_add_u32 s76, s46, 0x20000
	s_addc_u32 s77, s47, 0
	global_store_dwordx4 v4, v[64:67], s[76:77] sc1
	s_add_u32 s58, s52, 0x800
	s_addc_u32 s59, s53, 0
	global_load_dwordx4 v[16:19], v3, s[58:59] nt
	global_load_dwordx4 v[20:23], v3, s[58:59] offset:16 nt
	s_add_u32 s58, s52, 0x20800
	s_addc_u32 s59, s53, 0
	global_load_dwordx4 v[24:27], v3, s[58:59] nt
	global_load_dwordx4 v[28:31], v3, s[58:59] offset:16 nt
	s_add_u32 s58, s52, 0x40800
	s_addc_u32 s59, s53, 0
	global_load_dwordx4 v[32:35], v3, s[58:59] nt
	global_load_dwordx4 v[36:39], v3, s[58:59] offset:16 nt
	s_add_u32 s58, s52, 0x60800
	s_addc_u32 s59, s53, 0
	global_load_dwordx4 v[40:43], v3, s[58:59] nt
	global_load_dwordx4 v[44:47], v3, s[58:59] offset:16 nt
	s_add_u32 s58, s54, 0x800
	s_addc_u32 s59, s55, 0
	global_load_dwordx4 v[48:51], v3, s[58:59] nt
	global_load_dwordx4 v[52:55], v3, s[58:59] offset:16 nt
	s_add_u32 s58, s54, 0x20800
	s_addc_u32 s59, s55, 0
	global_load_dwordx4 v[56:59], v3, s[58:59] nt
	global_load_dwordx4 v[60:63], v3, s[58:59] offset:16 nt
	s_add_u32 s58, s54, 0x40800
	s_addc_u32 s59, s55, 0
	global_load_dwordx4 v[64:67], v3, s[58:59] nt
	global_load_dwordx4 v[68:71], v3, s[58:59] offset:16 nt
	s_waitcnt vmcnt(33)
	v_cvt_pk_f16_f32 v72, v72, v73
	v_cvt_pk_f16_f32 v73, v74, v75
	v_cvt_pk_f16_f32 v74, v76, v77
	v_cvt_pk_f16_f32 v75, v78, v79
	s_add_u32 s76, s44, 0x200
	s_addc_u32 s77, s45, 0
	global_store_dwordx4 v4, v[72:75], s[76:77] sc1
	s_waitcnt vmcnt(32)
	v_cvt_pk_f16_f32 v80, v80, v81
	v_cvt_pk_f16_f32 v81, v82, v83
	v_cvt_pk_f16_f32 v82, v84, v85
	v_cvt_pk_f16_f32 v83, v86, v87
	s_add_u32 s76, s44, 0x10200
	s_addc_u32 s77, s45, 0
	global_store_dwordx4 v4, v[80:83], s[76:77] sc1
	s_waitcnt vmcnt(31)
	v_cvt_pk_f16_f32 v88, v88, v89
	v_cvt_pk_f16_f32 v89, v90, v91
	v_cvt_pk_f16_f32 v90, v92, v93
	v_cvt_pk_f16_f32 v91, v94, v95
	s_add_u32 s76, s44, 0x20200
	s_addc_u32 s77, s45, 0
	global_store_dwordx4 v4, v[88:91], s[76:77] sc1
	s_waitcnt vmcnt(30)
	v_cvt_pk_f16_f32 v96, v96, v97
	v_cvt_pk_f16_f32 v97, v98, v99
	v_cvt_pk_f16_f32 v98, v100, v101
	v_cvt_pk_f16_f32 v99, v102, v103
	s_add_u32 s76, s44, 0x30200
	s_addc_u32 s77, s45, 0
	global_store_dwordx4 v4, v[96:99], s[76:77] sc1
	s_waitcnt vmcnt(29)
	v_cvt_pk_f16_f32 v104, v104, v105
	v_cvt_pk_f16_f32 v105, v106, v107
	v_cvt_pk_f16_f32 v106, v108, v109
	v_cvt_pk_f16_f32 v107, v110, v111
	s_add_u32 s76, s46, 0x200
	s_addc_u32 s77, s47, 0
	global_store_dwordx4 v4, v[104:107], s[76:77] sc1
	s_waitcnt vmcnt(28)
	v_cvt_pk_f16_f32 v112, v112, v113
	v_cvt_pk_f16_f32 v113, v114, v115
	v_cvt_pk_f16_f32 v114, v116, v117
	v_cvt_pk_f16_f32 v115, v118, v119
	s_add_u32 s76, s46, 0x10200
	s_addc_u32 s77, s47, 0
	global_store_dwordx4 v4, v[112:115], s[76:77] sc1
	s_waitcnt vmcnt(27)
	v_cvt_pk_f16_f32 v120, v120, v121
	v_cvt_pk_f16_f32 v121, v122, v123
	v_cvt_pk_f16_f32 v122, v124, v125
	v_cvt_pk_f16_f32 v123, v126, v127
	s_add_u32 s76, s46, 0x20200
	s_addc_u32 s77, s47, 0
	global_store_dwordx4 v4, v[120:123], s[76:77] sc1
	s_waitcnt vmcnt(21)
	s_barrier
	s_mov_b64 s[56:57], exec
	s_and_b64 exec, exec, s[78:79]
	global_store_dword v6, v5, s[48:49] offset:0 sc1
	s_mov_b64 exec, s[56:57]
	s_waitcnt vmcnt(20)
	v_cvt_pk_f16_f32 v16, v16, v17
	v_cvt_pk_f16_f32 v17, v18, v19
	v_cvt_pk_f16_f32 v18, v20, v21
	v_cvt_pk_f16_f32 v19, v22, v23
	s_add_u32 s76, s44, 0x400
	s_addc_u32 s77, s45, 0
	global_store_dwordx4 v4, v[16:19], s[76:77] sc1
	s_waitcnt vmcnt(19)
	v_cvt_pk_f16_f32 v24, v24, v25
	v_cvt_pk_f16_f32 v25, v26, v27
	v_cvt_pk_f16_f32 v26, v28, v29
	v_cvt_pk_f16_f32 v27, v30, v31
	s_add_u32 s76, s44, 0x10400
	s_addc_u32 s77, s45, 0
	global_store_dwordx4 v4, v[24:27], s[76:77] sc1
	s_waitcnt vmcnt(18)
	v_cvt_pk_f16_f32 v32, v32, v33
	v_cvt_pk_f16_f32 v33, v34, v35
	v_cvt_pk_f16_f32 v34, v36, v37
	v_cvt_pk_f16_f32 v35, v38, v39
	s_add_u32 s76, s44, 0x20400
	s_addc_u32 s77, s45, 0
	global_store_dwordx4 v4, v[32:35], s[76:77] sc1
	s_waitcnt vmcnt(17)
	v_cvt_pk_f16_f32 v40, v40, v41
	v_cvt_pk_f16_f32 v41, v42, v43
	v_cvt_pk_f16_f32 v42, v44, v45
	v_cvt_pk_f16_f32 v43, v46, v47
	s_add_u32 s76, s44, 0x30400
	s_addc_u32 s77, s45, 0
	global_store_dwordx4 v4, v[40:43], s[76:77] sc1
	s_waitcnt vmcnt(16)
	v_cvt_pk_f16_f32 v48, v48, v49
	v_cvt_pk_f16_f32 v49, v50, v51
	v_cvt_pk_f16_f32 v50, v52, v53
	v_cvt_pk_f16_f32 v51, v54, v55
	s_add_u32 s76, s46, 0x400
	s_addc_u32 s77, s47, 0
	global_store_dwordx4 v4, v[48:51], s[76:77] sc1
	s_waitcnt vmcnt(15)
	v_cvt_pk_f16_f32 v56, v56, v57
	v_cvt_pk_f16_f32 v57, v58, v59
	v_cvt_pk_f16_f32 v58, v60, v61
	v_cvt_pk_f16_f32 v59, v62, v63
	s_add_u32 s76, s46, 0x10400
	s_addc_u32 s77, s47, 0
	global_store_dwordx4 v4, v[56:59], s[76:77] sc1
	s_waitcnt vmcnt(14)
	v_cvt_pk_f16_f32 v64, v64, v65
	v_cvt_pk_f16_f32 v65, v66, v67
	v_cvt_pk_f16_f32 v66, v68, v69
	v_cvt_pk_f16_f32 v67, v70, v71
	s_add_u32 s76, s46, 0x20400
	s_addc_u32 s77, s47, 0
	global_store_dwordx4 v4, v[64:67], s[76:77] sc1
	s_waitcnt vmcnt(8)
	s_barrier
	s_mov_b64 s[56:57], exec
	s_and_b64 exec, exec, s[78:79]
	global_store_dword v6, v5, s[48:49] offset:256 sc1
	s_mov_b64 exec, s[56:57]
	s_waitcnt vmcnt(1)
	s_barrier
	s_mov_b64 s[56:57], exec
	s_and_b64 exec, exec, s[78:79]
	global_store_dword v6, v5, s[48:49] offset:512 sc1
	s_mov_b64 exec, s[56:57]
	s_mov_b32 s24, s2
	s_lshl_b32 s20, s24, 4
	s_lshl_b32 s0, s24, 5
	s_ashr_i32 s21, s20, 31
	s_and_b32 s25, s0, 0xffffffc0
	s_lshl_b64 s[20:21], s[20:21], 2
	v_lshrrev_b32_e32 v6, 6, v0
	s_waitcnt lgkmcnt(0)
	s_add_u32 s26, s30, s20
	s_addc_u32 s27, s31, s21
	v_lshl_or_b32 v2, v6, 3, s25
	s_and_b32 s25, s2, 1
	s_lshl_b32 s2, s25, 7
	s_add_u32 s20, s28, s2
	v_and_b32_e32 v7, 63, v0
	s_mov_b32 s3, 0
	s_addc_u32 s21, s29, 0
	s_bfe_u32 s2, s24, 0x1a0001
	v_add_u32_e32 v2, v2, v7
	v_mov_b32_e32 v3, 0
	s_lshl_b64 s[2:3], s[2:3], 19
	v_lshl_add_u32 v1, v6, 2, 0
	v_lshlrev_b64 v[4:5], 8, v[2:3]
	v_lshl_or_b32 v2, v6, 16, s2
	s_lshl_b32 s2, s25, 12
	v_lshlrev_b32_e32 v6, 2, v7
	v_cmp_gt_u32_e64 s[0:1], 8, v7
	v_cmp_eq_u32_e64 s[22:23], 0, v7
	v_cmp_eq_u32_e64 s[6:7], 1, v7
	v_cmp_eq_u32_e64 s[8:9], 2, v7
	v_cmp_eq_u32_e64 s[10:11], 3, v7
	v_cmp_eq_u32_e64 s[12:13], 4, v7
	v_cmp_eq_u32_e64 s[14:15], 5, v7
	v_cmp_eq_u32_e64 s[16:17], 6, v7
	v_cmp_eq_u32_e64 s[18:19], 7, v7
	v_or3_b32 v6, v2, s2, v6
	v_mov_b32_e32 v7, s3
	v_cmp_eq_u32_e64 s[4:5], 0, v0
	v_lshl_add_u64 v[4:5], s[20:21], 0, v[4:5]
	v_lshl_add_u64 v[6:7], s[42:43], 0, v[6:7]
	s_mov_b64 s[28:29], 0
	s_lshr_b32 s58, s24, 1
	s_lshl_b32 s58, s58, 19
	s_add_u32 s60, s42, s58
	s_addc_u32 s61, s43, 0
	s_add_u32 s62, s60, 0x2000
	s_addc_u32 s63, s61, 0
	s_add_u32 s64, s62, 0x2000
	s_addc_u32 s65, s63, 0
	s_add_u32 s66, s64, 0x2000
	s_addc_u32 s67, s65, 0
	s_add_u32 s68, s66, 0x2000
	s_addc_u32 s69, s67, 0
	s_add_u32 s70, s68, 0x2000
	s_addc_u32 s71, s69, 0
	s_add_u32 s72, s70, 0x2000
	s_addc_u32 s73, s71, 0
	s_add_u32 s74, s72, 0x2000
	s_addc_u32 s75, s73, 0
	v_lshrrev_b32_e32 v96, 6, v0
	v_lshlrev_b32_e32 v96, 16, v96
	v_and_b32_e32 v97, 63, v0
	v_lshl_add_u32 v96, v97, 2, v96
	s_and_b32 s59, s24, 1
	s_lshl_b32 s59, s59, 12
	v_add_u32_e32 v96, s59, v96
	s_mov_b32 s76, 0
	s_mov_b32 s77, 0
	global_load_dword v100, v96, s[60:61] offset:0 nt
	global_load_dword v101, v96, s[62:63] offset:0 nt
	global_load_dword v102, v96, s[64:65] offset:0 nt
	global_load_dword v103, v96, s[66:67] offset:0 nt
	global_load_dword v104, v96, s[68:69] offset:0 nt
	global_load_dword v105, v96, s[70:71] offset:0 nt
	global_load_dword v106, v96, s[72:73] offset:0 nt
	global_load_dword v107, v96, s[74:75] offset:0 nt
	global_load_dword v108, v96, s[60:61] offset:256 nt
	global_load_dword v109, v96, s[62:63] offset:256 nt
	global_load_dword v110, v96, s[64:65] offset:256 nt
	global_load_dword v111, v96, s[66:67] offset:256 nt
	global_load_dword v112, v96, s[68:69] offset:256 nt
	global_load_dword v113, v96, s[70:71] offset:256 nt
	global_load_dword v114, v96, s[72:73] offset:256 nt
	global_load_dword v115, v96, s[74:75] offset:256 nt
	global_load_dword v116, v96, s[60:61] offset:512 nt
	global_load_dword v117, v96, s[62:63] offset:512 nt
	global_load_dword v118, v96, s[64:65] offset:512 nt
	global_load_dword v119, v96, s[66:67] offset:512 nt
	global_load_dword v120, v96, s[68:69] offset:512 nt
	global_load_dword v121, v96, s[70:71] offset:512 nt
	global_load_dword v122, v96, s[72:73] offset:512 nt
	global_load_dword v123, v96, s[74:75] offset:512 nt
	global_load_dword v124, v96, s[60:61] offset:768 nt
	global_load_dword v125, v96, s[62:63] offset:768 nt
	global_load_dword v126, v96, s[64:65] offset:768 nt
	global_load_dword v127, v96, s[66:67] offset:768 nt
	global_load_dword v128, v96, s[68:69] offset:768 nt
	global_load_dword v129, v96, s[70:71] offset:768 nt
	global_load_dword v130, v96, s[72:73] offset:768 nt
	global_load_dword v131, v96, s[74:75] offset:768 nt
	global_load_dword v132, v96, s[60:61] offset:1024 nt
	global_load_dword v133, v96, s[62:63] offset:1024 nt
	global_load_dword v134, v96, s[64:65] offset:1024 nt
	global_load_dword v135, v96, s[66:67] offset:1024 nt
	global_load_dword v136, v96, s[68:69] offset:1024 nt
	global_load_dword v137, v96, s[70:71] offset:1024 nt
	global_load_dword v138, v96, s[72:73] offset:1024 nt
	global_load_dword v139, v96, s[74:75] offset:1024 nt
	global_load_dword v140, v96, s[60:61] offset:1280 nt
	global_load_dword v141, v96, s[62:63] offset:1280 nt
	global_load_dword v142, v96, s[64:65] offset:1280 nt
	global_load_dword v143, v96, s[66:67] offset:1280 nt
	global_load_dword v144, v96, s[68:69] offset:1280 nt
	global_load_dword v145, v96, s[70:71] offset:1280 nt
	global_load_dword v146, v96, s[72:73] offset:1280 nt
	global_load_dword v147, v96, s[74:75] offset:1280 nt
	global_load_dword v148, v96, s[60:61] offset:1536 nt
	global_load_dword v149, v96, s[62:63] offset:1536 nt
	global_load_dword v150, v96, s[64:65] offset:1536 nt
	global_load_dword v151, v96, s[66:67] offset:1536 nt
	global_load_dword v152, v96, s[68:69] offset:1536 nt
	global_load_dword v153, v96, s[70:71] offset:1536 nt
	global_load_dword v154, v96, s[72:73] offset:1536 nt
	global_load_dword v155, v96, s[74:75] offset:1536 nt
	s_waitcnt vmcnt(48)
	v_cmp_ne_u32_e32 vcc, 0, v100
	s_nop 1
	v_mov_b32_e32 v2, vcc_lo
	v_mov_b32_e32 v9, vcc_hi
	v_cmp_ne_u32_e32 vcc, 0, v101
	v_cndmask_b32_e64 v2, 0, v2, s[22:23]
	v_cndmask_b32_e64 v9, 0, v9, s[22:23]
	v_mov_b32_e32 v11, vcc_hi
	v_mov_b32_e32 v14, vcc_lo
	v_cndmask_b32_e64 v9, v9, v11, s[6:7]
	v_cndmask_b32_e64 v2, v2, v14, s[6:7]
	v_cmp_ne_u32_e32 vcc, 0, v102
	s_nop 1
	v_mov_b32_e32 v11, vcc_lo
	v_mov_b32_e32 v14, vcc_hi
	v_cmp_ne_u32_e32 vcc, 0, v103
	v_cndmask_b32_e64 v2, v2, v11, s[8:9]
	v_cndmask_b32_e64 v9, v9, v14, s[8:9]
	v_mov_b32_e32 v11, vcc_hi
	v_mov_b32_e32 v14, vcc_lo
	v_cmp_ne_u32_e32 vcc, 0, v104
	v_cndmask_b32_e64 v9, v9, v11, s[10:11]
	v_cndmask_b32_e64 v2, v2, v14, s[10:11]
	v_mov_b32_e32 v11, vcc_lo
	v_mov_b32_e32 v12, vcc_hi
	v_cmp_ne_u32_e32 vcc, 0, v105
	v_cndmask_b32_e64 v2, v2, v11, s[12:13]
	v_cndmask_b32_e64 v9, v9, v12, s[12:13]
	v_mov_b32_e32 v11, vcc_hi
	v_mov_b32_e32 v12, vcc_lo
	v_cndmask_b32_e64 v9, v9, v11, s[14:15]
	v_cndmask_b32_e64 v2, v2, v12, s[14:15]
	v_cmp_ne_u32_e32 vcc, 0, v106
	s_nop 1
	v_mov_b32_e32 v10, vcc_lo
	v_mov_b32_e32 v11, vcc_hi
	v_cmp_ne_u32_e32 vcc, 0, v107
	v_cndmask_b32_e64 v2, v2, v10, s[16:17]
	v_cndmask_b32_e64 v8, v9, v11, s[16:17]
	v_mov_b32_e32 v9, vcc_hi
	v_mov_b32_e32 v10, vcc_lo
	v_cndmask_b32_e64 v9, v8, v9, s[18:19]
	v_cndmask_b32_e64 v8, v2, v10, s[18:19]
	s_mov_b64 s[2:3], exec
	s_mov_b64 exec, s[0:1]
	global_store_dwordx2 v[4:5], v[8:9], off
	s_mov_b64 exec, s[2:3]
	v_cmp_ne_u64_e32 vcc, 0, v[8:9]
	s_and_b64 s[20:21], s[0:1], vcc
	s_cmp_lg_u64 s[20:21], 0
	s_cselect_b32 s20, 1, 0
	s_or_b32 s76, s76, s20
	v_cmp_ne_u64_e32 vcc, -1, v[8:9]
	s_and_b64 s[20:21], s[0:1], vcc
	s_cmp_lg_u64 s[20:21], 0
	s_cselect_b32 s20, 1, 0
	s_or_b32 s77, s77, s20
	v_lshl_add_u64 v[4:5], v[4:5], 0, 8
	global_load_dword v156, v96, s[60:61] offset:1792 nt
	global_load_dword v157, v96, s[62:63] offset:1792 nt
	global_load_dword v158, v96, s[64:65] offset:1792 nt
	global_load_dword v159, v96, s[66:67] offset:1792 nt
	global_load_dword v160, v96, s[68:69] offset:1792 nt
	global_load_dword v161, v96, s[70:71] offset:1792 nt
	global_load_dword v162, v96, s[72:73] offset:1792 nt
	global_load_dword v163, v96, s[74:75] offset:1792 nt
	s_waitcnt vmcnt(49)
	v_cmp_ne_u32_e32 vcc, 0, v108
	s_nop 1
	v_mov_b32_e32 v2, vcc_lo
	v_mov_b32_e32 v9, vcc_hi
	v_cmp_ne_u32_e32 vcc, 0, v109
	v_cndmask_b32_e64 v2, 0, v2, s[22:23]
	v_cndmask_b32_e64 v9, 0, v9, s[22:23]
	v_mov_b32_e32 v11, vcc_hi
	v_mov_b32_e32 v14, vcc_lo
	v_cndmask_b32_e64 v9, v9, v11, s[6:7]
	v_cndmask_b32_e64 v2, v2, v14, s[6:7]
	v_cmp_ne_u32_e32 vcc, 0, v110
	s_nop 1
	v_mov_b32_e32 v11, vcc_lo
	v_mov_b32_e32 v14, vcc_hi
	v_cmp_ne_u32_e32 vcc, 0, v111
	v_cndmask_b32_e64 v2, v2, v11, s[8:9]
	v_cndmask_b32_e64 v9, v9, v14, s[8:9]
	v_mov_b32_e32 v11, vcc_hi
	v_mov_b32_e32 v14, vcc_lo
	v_cmp_ne_u32_e32 vcc, 0, v112
	v_cndmask_b32_e64 v9, v9, v11, s[10:11]
	v_cndmask_b32_e64 v2, v2, v14, s[10:11]
	v_mov_b32_e32 v11, vcc_lo
	v_mov_b32_e32 v12, vcc_hi
	v_cmp_ne_u32_e32 vcc, 0, v113
	v_cndmask_b32_e64 v2, v2, v11, s[12:13]
	v_cndmask_b32_e64 v9, v9, v12, s[12:13]
	v_mov_b32_e32 v11, vcc_hi
	v_mov_b32_e32 v12, vcc_lo
	v_cndmask_b32_e64 v9, v9, v11, s[14:15]
	v_cndmask_b32_e64 v2, v2, v12, s[14:15]
	v_cmp_ne_u32_e32 vcc, 0, v114
	s_nop 1
	v_mov_b32_e32 v10, vcc_lo
	v_mov_b32_e32 v11, vcc_hi
	v_cmp_ne_u32_e32 vcc, 0, v115
	v_cndmask_b32_e64 v2, v2, v10, s[16:17]
	v_cndmask_b32_e64 v8, v9, v11, s[16:17]
	v_mov_b32_e32 v9, vcc_hi
	v_mov_b32_e32 v10, vcc_lo
	v_cndmask_b32_e64 v9, v8, v9, s[18:19]
	v_cndmask_b32_e64 v8, v2, v10, s[18:19]
	s_mov_b64 s[2:3], exec
	s_mov_b64 exec, s[0:1]
	global_store_dwordx2 v[4:5], v[8:9], off
	s_mov_b64 exec, s[2:3]
	v_cmp_ne_u64_e32 vcc, 0, v[8:9]
	s_and_b64 s[20:21], s[0:1], vcc
	s_cmp_lg_u64 s[20:21], 0
	s_cselect_b32 s20, 2, 0
	s_or_b32 s76, s76, s20
	v_cmp_ne_u64_e32 vcc, -1, v[8:9]
	s_and_b64 s[20:21], s[0:1], vcc
	s_cmp_lg_u64 s[20:21], 0
	s_cselect_b32 s20, 2, 0
	s_or_b32 s77, s77, s20
	v_lshl_add_u64 v[4:5], v[4:5], 0, 8
	global_load_dword v164, v96, s[60:61] offset:2048 nt
	global_load_dword v165, v96, s[62:63] offset:2048 nt
	global_load_dword v166, v96, s[64:65] offset:2048 nt
	global_load_dword v167, v96, s[66:67] offset:2048 nt
	global_load_dword v168, v96, s[68:69] offset:2048 nt
	global_load_dword v169, v96, s[70:71] offset:2048 nt
	global_load_dword v170, v96, s[72:73] offset:2048 nt
	global_load_dword v171, v96, s[74:75] offset:2048 nt
	s_waitcnt vmcnt(50)
	v_cmp_ne_u32_e32 vcc, 0, v116
	s_nop 1
	v_mov_b32_e32 v2, vcc_lo
	v_mov_b32_e32 v9, vcc_hi
	v_cmp_ne_u32_e32 vcc, 0, v117
	v_cndmask_b32_e64 v2, 0, v2, s[22:23]
	v_cndmask_b32_e64 v9, 0, v9, s[22:23]
	v_mov_b32_e32 v11, vcc_hi
	v_mov_b32_e32 v14, vcc_lo
	v_cndmask_b32_e64 v9, v9, v11, s[6:7]
	v_cndmask_b32_e64 v2, v2, v14, s[6:7]
	v_cmp_ne_u32_e32 vcc, 0, v118
	s_nop 1
	v_mov_b32_e32 v11, vcc_lo
	v_mov_b32_e32 v14, vcc_hi
	v_cmp_ne_u32_e32 vcc, 0, v119
	v_cndmask_b32_e64 v2, v2, v11, s[8:9]
	v_cndmask_b32_e64 v9, v9, v14, s[8:9]
	v_mov_b32_e32 v11, vcc_hi
	v_mov_b32_e32 v14, vcc_lo
	v_cmp_ne_u32_e32 vcc, 0, v120
	v_cndmask_b32_e64 v9, v9, v11, s[10:11]
	v_cndmask_b32_e64 v2, v2, v14, s[10:11]
	v_mov_b32_e32 v11, vcc_lo
	v_mov_b32_e32 v12, vcc_hi
	v_cmp_ne_u32_e32 vcc, 0, v121
	v_cndmask_b32_e64 v2, v2, v11, s[12:13]
	v_cndmask_b32_e64 v9, v9, v12, s[12:13]
	v_mov_b32_e32 v11, vcc_hi
	v_mov_b32_e32 v12, vcc_lo
	v_cndmask_b32_e64 v9, v9, v11, s[14:15]
	v_cndmask_b32_e64 v2, v2, v12, s[14:15]
	v_cmp_ne_u32_e32 vcc, 0, v122
	s_nop 1
	v_mov_b32_e32 v10, vcc_lo
	v_mov_b32_e32 v11, vcc_hi
	v_cmp_ne_u32_e32 vcc, 0, v123
	v_cndmask_b32_e64 v2, v2, v10, s[16:17]
	v_cndmask_b32_e64 v8, v9, v11, s[16:17]
	v_mov_b32_e32 v9, vcc_hi
	v_mov_b32_e32 v10, vcc_lo
	v_cndmask_b32_e64 v9, v8, v9, s[18:19]
	v_cndmask_b32_e64 v8, v2, v10, s[18:19]
	s_mov_b64 s[2:3], exec
	s_mov_b64 exec, s[0:1]
	global_store_dwordx2 v[4:5], v[8:9], off
	s_mov_b64 exec, s[2:3]
	v_cmp_ne_u64_e32 vcc, 0, v[8:9]
	s_and_b64 s[20:21], s[0:1], vcc
	s_cmp_lg_u64 s[20:21], 0
	s_cselect_b32 s20, 4, 0
	s_or_b32 s76, s76, s20
	v_cmp_ne_u64_e32 vcc, -1, v[8:9]
	s_and_b64 s[20:21], s[0:1], vcc
	s_cmp_lg_u64 s[20:21], 0
	s_cselect_b32 s20, 4, 0
	s_or_b32 s77, s77, s20
	v_lshl_add_u64 v[4:5], v[4:5], 0, 8
	global_load_dword v172, v96, s[60:61] offset:2304 nt
	global_load_dword v173, v96, s[62:63] offset:2304 nt
	global_load_dword v174, v96, s[64:65] offset:2304 nt
	global_load_dword v175, v96, s[66:67] offset:2304 nt
	global_load_dword v176, v96, s[68:69] offset:2304 nt
	global_load_dword v177, v96, s[70:71] offset:2304 nt
	global_load_dword v178, v96, s[72:73] offset:2304 nt
	global_load_dword v179, v96, s[74:75] offset:2304 nt
	s_waitcnt vmcnt(51)
	v_cmp_ne_u32_e32 vcc, 0, v124
	s_nop 1
	v_mov_b32_e32 v2, vcc_lo
	v_mov_b32_e32 v9, vcc_hi
	v_cmp_ne_u32_e32 vcc, 0, v125
	v_cndmask_b32_e64 v2, 0, v2, s[22:23]
	v_cndmask_b32_e64 v9, 0, v9, s[22:23]
	v_mov_b32_e32 v11, vcc_hi
	v_mov_b32_e32 v14, vcc_lo
	v_cndmask_b32_e64 v9, v9, v11, s[6:7]
	v_cndmask_b32_e64 v2, v2, v14, s[6:7]
	v_cmp_ne_u32_e32 vcc, 0, v126
	s_nop 1
	v_mov_b32_e32 v11, vcc_lo
	v_mov_b32_e32 v14, vcc_hi
	v_cmp_ne_u32_e32 vcc, 0, v127
	v_cndmask_b32_e64 v2, v2, v11, s[8:9]
	v_cndmask_b32_e64 v9, v9, v14, s[8:9]
	v_mov_b32_e32 v11, vcc_hi
	v_mov_b32_e32 v14, vcc_lo
	v_cmp_ne_u32_e32 vcc, 0, v128
	v_cndmask_b32_e64 v9, v9, v11, s[10:11]
	v_cndmask_b32_e64 v2, v2, v14, s[10:11]
	v_mov_b32_e32 v11, vcc_lo
	v_mov_b32_e32 v12, vcc_hi
	v_cmp_ne_u32_e32 vcc, 0, v129
	v_cndmask_b32_e64 v2, v2, v11, s[12:13]
	v_cndmask_b32_e64 v9, v9, v12, s[12:13]
	v_mov_b32_e32 v11, vcc_hi
	v_mov_b32_e32 v12, vcc_lo
	v_cndmask_b32_e64 v9, v9, v11, s[14:15]
	v_cndmask_b32_e64 v2, v2, v12, s[14:15]
	v_cmp_ne_u32_e32 vcc, 0, v130
	s_nop 1
	v_mov_b32_e32 v10, vcc_lo
	v_mov_b32_e32 v11, vcc_hi
	v_cmp_ne_u32_e32 vcc, 0, v131
	v_cndmask_b32_e64 v2, v2, v10, s[16:17]
	v_cndmask_b32_e64 v8, v9, v11, s[16:17]
	v_mov_b32_e32 v9, vcc_hi
	v_mov_b32_e32 v10, vcc_lo
	v_cndmask_b32_e64 v9, v8, v9, s[18:19]
	v_cndmask_b32_e64 v8, v2, v10, s[18:19]
	s_mov_b64 s[2:3], exec
	s_mov_b64 exec, s[0:1]
	global_store_dwordx2 v[4:5], v[8:9], off
	s_mov_b64 exec, s[2:3]
	v_cmp_ne_u64_e32 vcc, 0, v[8:9]
	s_and_b64 s[20:21], s[0:1], vcc
	s_cmp_lg_u64 s[20:21], 0
	s_cselect_b32 s20, 8, 0
	s_or_b32 s76, s76, s20
	v_cmp_ne_u64_e32 vcc, -1, v[8:9]
	s_and_b64 s[20:21], s[0:1], vcc
	s_cmp_lg_u64 s[20:21], 0
	s_cselect_b32 s20, 8, 0
	s_or_b32 s77, s77, s20
	v_lshl_add_u64 v[4:5], v[4:5], 0, 8
	global_load_dword v180, v96, s[60:61] offset:2560 nt
	global_load_dword v181, v96, s[62:63] offset:2560 nt
	global_load_dword v182, v96, s[64:65] offset:2560 nt
	global_load_dword v183, v96, s[66:67] offset:2560 nt
	global_load_dword v184, v96, s[68:69] offset:2560 nt
	global_load_dword v185, v96, s[70:71] offset:2560 nt
	global_load_dword v186, v96, s[72:73] offset:2560 nt
	global_load_dword v187, v96, s[74:75] offset:2560 nt
	s_waitcnt vmcnt(52)
	v_cmp_ne_u32_e32 vcc, 0, v132
	s_nop 1
	v_mov_b32_e32 v2, vcc_lo
	v_mov_b32_e32 v9, vcc_hi
	v_cmp_ne_u32_e32 vcc, 0, v133
	v_cndmask_b32_e64 v2, 0, v2, s[22:23]
	v_cndmask_b32_e64 v9, 0, v9, s[22:23]
	v_mov_b32_e32 v11, vcc_hi
	v_mov_b32_e32 v14, vcc_lo
	v_cndmask_b32_e64 v9, v9, v11, s[6:7]
	v_cndmask_b32_e64 v2, v2, v14, s[6:7]
	v_cmp_ne_u32_e32 vcc, 0, v134
	s_nop 1
	v_mov_b32_e32 v11, vcc_lo
	v_mov_b32_e32 v14, vcc_hi
	v_cmp_ne_u32_e32 vcc, 0, v135
	v_cndmask_b32_e64 v2, v2, v11, s[8:9]
	v_cndmask_b32_e64 v9, v9, v14, s[8:9]
	v_mov_b32_e32 v11, vcc_hi
	v_mov_b32_e32 v14, vcc_lo
	v_cmp_ne_u32_e32 vcc, 0, v136
	v_cndmask_b32_e64 v9, v9, v11, s[10:11]
	v_cndmask_b32_e64 v2, v2, v14, s[10:11]
	v_mov_b32_e32 v11, vcc_lo
	v_mov_b32_e32 v12, vcc_hi
	v_cmp_ne_u32_e32 vcc, 0, v137
	v_cndmask_b32_e64 v2, v2, v11, s[12:13]
	v_cndmask_b32_e64 v9, v9, v12, s[12:13]
	v_mov_b32_e32 v11, vcc_hi
	v_mov_b32_e32 v12, vcc_lo
	v_cndmask_b32_e64 v9, v9, v11, s[14:15]
	v_cndmask_b32_e64 v2, v2, v12, s[14:15]
	v_cmp_ne_u32_e32 vcc, 0, v138
	s_nop 1
	v_mov_b32_e32 v10, vcc_lo
	v_mov_b32_e32 v11, vcc_hi
	v_cmp_ne_u32_e32 vcc, 0, v139
	v_cndmask_b32_e64 v2, v2, v10, s[16:17]
	v_cndmask_b32_e64 v8, v9, v11, s[16:17]
	v_mov_b32_e32 v9, vcc_hi
	v_mov_b32_e32 v10, vcc_lo
	v_cndmask_b32_e64 v9, v8, v9, s[18:19]
	v_cndmask_b32_e64 v8, v2, v10, s[18:19]
	s_mov_b64 s[2:3], exec
	s_mov_b64 exec, s[0:1]
	global_store_dwordx2 v[4:5], v[8:9], off
	s_mov_b64 exec, s[2:3]
	v_cmp_ne_u64_e32 vcc, 0, v[8:9]
	s_and_b64 s[20:21], s[0:1], vcc
	s_cmp_lg_u64 s[20:21], 0
	s_cselect_b32 s20, 16, 0
	s_or_b32 s76, s76, s20
	v_cmp_ne_u64_e32 vcc, -1, v[8:9]
	s_and_b64 s[20:21], s[0:1], vcc
	s_cmp_lg_u64 s[20:21], 0
	s_cselect_b32 s20, 16, 0
	s_or_b32 s77, s77, s20
	v_lshl_add_u64 v[4:5], v[4:5], 0, 8
	global_load_dword v188, v96, s[60:61] offset:2816 nt
	global_load_dword v189, v96, s[62:63] offset:2816 nt
	global_load_dword v190, v96, s[64:65] offset:2816 nt
	global_load_dword v191, v96, s[66:67] offset:2816 nt
	global_load_dword v192, v96, s[68:69] offset:2816 nt
	global_load_dword v193, v96, s[70:71] offset:2816 nt
	global_load_dword v194, v96, s[72:73] offset:2816 nt
	global_load_dword v195, v96, s[74:75] offset:2816 nt
	s_waitcnt vmcnt(53)
	v_cmp_ne_u32_e32 vcc, 0, v140
	s_nop 1
	v_mov_b32_e32 v2, vcc_lo
	v_mov_b32_e32 v9, vcc_hi
	v_cmp_ne_u32_e32 vcc, 0, v141
	v_cndmask_b32_e64 v2, 0, v2, s[22:23]
	v_cndmask_b32_e64 v9, 0, v9, s[22:23]
	v_mov_b32_e32 v11, vcc_hi
	v_mov_b32_e32 v14, vcc_lo
	v_cndmask_b32_e64 v9, v9, v11, s[6:7]
	v_cndmask_b32_e64 v2, v2, v14, s[6:7]
	v_cmp_ne_u32_e32 vcc, 0, v142
	s_nop 1
	v_mov_b32_e32 v11, vcc_lo
	v_mov_b32_e32 v14, vcc_hi
	v_cmp_ne_u32_e32 vcc, 0, v143
	v_cndmask_b32_e64 v2, v2, v11, s[8:9]
	v_cndmask_b32_e64 v9, v9, v14, s[8:9]
	v_mov_b32_e32 v11, vcc_hi
	v_mov_b32_e32 v14, vcc_lo
	v_cmp_ne_u32_e32 vcc, 0, v144
	v_cndmask_b32_e64 v9, v9, v11, s[10:11]
	v_cndmask_b32_e64 v2, v2, v14, s[10:11]
	v_mov_b32_e32 v11, vcc_lo
	v_mov_b32_e32 v12, vcc_hi
	v_cmp_ne_u32_e32 vcc, 0, v145
	v_cndmask_b32_e64 v2, v2, v11, s[12:13]
	v_cndmask_b32_e64 v9, v9, v12, s[12:13]
	v_mov_b32_e32 v11, vcc_hi
	v_mov_b32_e32 v12, vcc_lo
	v_cndmask_b32_e64 v9, v9, v11, s[14:15]
	v_cndmask_b32_e64 v2, v2, v12, s[14:15]
	v_cmp_ne_u32_e32 vcc, 0, v146
	s_nop 1
	v_mov_b32_e32 v10, vcc_lo
	v_mov_b32_e32 v11, vcc_hi
	v_cmp_ne_u32_e32 vcc, 0, v147
	v_cndmask_b32_e64 v2, v2, v10, s[16:17]
	v_cndmask_b32_e64 v8, v9, v11, s[16:17]
	v_mov_b32_e32 v9, vcc_hi
	v_mov_b32_e32 v10, vcc_lo
	v_cndmask_b32_e64 v9, v8, v9, s[18:19]
	v_cndmask_b32_e64 v8, v2, v10, s[18:19]
	s_mov_b64 s[2:3], exec
	s_mov_b64 exec, s[0:1]
	global_store_dwordx2 v[4:5], v[8:9], off
	s_mov_b64 exec, s[2:3]
	v_cmp_ne_u64_e32 vcc, 0, v[8:9]
	s_and_b64 s[20:21], s[0:1], vcc
	s_cmp_lg_u64 s[20:21], 0
	s_cselect_b32 s20, 32, 0
	s_or_b32 s76, s76, s20
	v_cmp_ne_u64_e32 vcc, -1, v[8:9]
	s_and_b64 s[20:21], s[0:1], vcc
	s_cmp_lg_u64 s[20:21], 0
	s_cselect_b32 s20, 32, 0
	s_or_b32 s77, s77, s20
	v_lshl_add_u64 v[4:5], v[4:5], 0, 8
	global_load_dword v196, v96, s[60:61] offset:3072 nt
	global_load_dword v197, v96, s[62:63] offset:3072 nt
	global_load_dword v198, v96, s[64:65] offset:3072 nt
	global_load_dword v199, v96, s[66:67] offset:3072 nt
	global_load_dword v200, v96, s[68:69] offset:3072 nt
	global_load_dword v201, v96, s[70:71] offset:3072 nt
	global_load_dword v202, v96, s[72:73] offset:3072 nt
	global_load_dword v203, v96, s[74:75] offset:3072 nt
	s_waitcnt vmcnt(54)
	v_cmp_ne_u32_e32 vcc, 0, v148
	s_nop 1
	v_mov_b32_e32 v2, vcc_lo
	v_mov_b32_e32 v9, vcc_hi
	v_cmp_ne_u32_e32 vcc, 0, v149
	v_cndmask_b32_e64 v2, 0, v2, s[22:23]
	v_cndmask_b32_e64 v9, 0, v9, s[22:23]
	v_mov_b32_e32 v11, vcc_hi
	v_mov_b32_e32 v14, vcc_lo
	v_cndmask_b32_e64 v9, v9, v11, s[6:7]
	v_cndmask_b32_e64 v2, v2, v14, s[6:7]
	v_cmp_ne_u32_e32 vcc, 0, v150
	s_nop 1
	v_mov_b32_e32 v11, vcc_lo
	v_mov_b32_e32 v14, vcc_hi
	v_cmp_ne_u32_e32 vcc, 0, v151
	v_cndmask_b32_e64 v2, v2, v11, s[8:9]
	v_cndmask_b32_e64 v9, v9, v14, s[8:9]
	v_mov_b32_e32 v11, vcc_hi
	v_mov_b32_e32 v14, vcc_lo
	v_cmp_ne_u32_e32 vcc, 0, v152
	v_cndmask_b32_e64 v9, v9, v11, s[10:11]
	v_cndmask_b32_e64 v2, v2, v14, s[10:11]
	v_mov_b32_e32 v11, vcc_lo
	v_mov_b32_e32 v12, vcc_hi
	v_cmp_ne_u32_e32 vcc, 0, v153
	v_cndmask_b32_e64 v2, v2, v11, s[12:13]
	v_cndmask_b32_e64 v9, v9, v12, s[12:13]
	v_mov_b32_e32 v11, vcc_hi
	v_mov_b32_e32 v12, vcc_lo
	v_cndmask_b32_e64 v9, v9, v11, s[14:15]
	v_cndmask_b32_e64 v2, v2, v12, s[14:15]
	v_cmp_ne_u32_e32 vcc, 0, v154
	s_nop 1
	v_mov_b32_e32 v10, vcc_lo
	v_mov_b32_e32 v11, vcc_hi
	v_cmp_ne_u32_e32 vcc, 0, v155
	v_cndmask_b32_e64 v2, v2, v10, s[16:17]
	v_cndmask_b32_e64 v8, v9, v11, s[16:17]
	v_mov_b32_e32 v9, vcc_hi
	v_mov_b32_e32 v10, vcc_lo
	v_cndmask_b32_e64 v9, v8, v9, s[18:19]
	v_cndmask_b32_e64 v8, v2, v10, s[18:19]
	s_mov_b64 s[2:3], exec
	s_mov_b64 exec, s[0:1]
	global_store_dwordx2 v[4:5], v[8:9], off
	s_mov_b64 exec, s[2:3]
	v_cmp_ne_u64_e32 vcc, 0, v[8:9]
	s_and_b64 s[20:21], s[0:1], vcc
	s_cmp_lg_u64 s[20:21], 0
	s_cselect_b32 s20, 64, 0
	s_or_b32 s76, s76, s20
	v_cmp_ne_u64_e32 vcc, -1, v[8:9]
	s_and_b64 s[20:21], s[0:1], vcc
	s_cmp_lg_u64 s[20:21], 0
	s_cselect_b32 s20, 64, 0
	s_or_b32 s77, s77, s20
	v_lshl_add_u64 v[4:5], v[4:5], 0, 8
	global_load_dword v204, v96, s[60:61] offset:3328 nt
	global_load_dword v205, v96, s[62:63] offset:3328 nt
	global_load_dword v206, v96, s[64:65] offset:3328 nt
	global_load_dword v207, v96, s[66:67] offset:3328 nt
	global_load_dword v208, v96, s[68:69] offset:3328 nt
	global_load_dword v209, v96, s[70:71] offset:3328 nt
	global_load_dword v210, v96, s[72:73] offset:3328 nt
	global_load_dword v211, v96, s[74:75] offset:3328 nt
	s_waitcnt vmcnt(54)
	v_cmp_ne_u32_e32 vcc, 0, v156
	s_nop 1
	v_mov_b32_e32 v2, vcc_lo
	v_mov_b32_e32 v9, vcc_hi
	v_cmp_ne_u32_e32 vcc, 0, v157
	v_cndmask_b32_e64 v2, 0, v2, s[22:23]
	v_cndmask_b32_e64 v9, 0, v9, s[22:23]
	v_mov_b32_e32 v11, vcc_hi
	v_mov_b32_e32 v14, vcc_lo
	v_cndmask_b32_e64 v9, v9, v11, s[6:7]
	v_cndmask_b32_e64 v2, v2, v14, s[6:7]
	v_cmp_ne_u32_e32 vcc, 0, v158
	s_nop 1
	v_mov_b32_e32 v11, vcc_lo
	v_mov_b32_e32 v14, vcc_hi
	v_cmp_ne_u32_e32 vcc, 0, v159
	v_cndmask_b32_e64 v2, v2, v11, s[8:9]
	v_cndmask_b32_e64 v9, v9, v14, s[8:9]
	v_mov_b32_e32 v11, vcc_hi
	v_mov_b32_e32 v14, vcc_lo
	v_cmp_ne_u32_e32 vcc, 0, v160
	v_cndmask_b32_e64 v9, v9, v11, s[10:11]
	v_cndmask_b32_e64 v2, v2, v14, s[10:11]
	v_mov_b32_e32 v11, vcc_lo
	v_mov_b32_e32 v12, vcc_hi
	v_cmp_ne_u32_e32 vcc, 0, v161
	v_cndmask_b32_e64 v2, v2, v11, s[12:13]
	v_cndmask_b32_e64 v9, v9, v12, s[12:13]
	v_mov_b32_e32 v11, vcc_hi
	v_mov_b32_e32 v12, vcc_lo
	v_cndmask_b32_e64 v9, v9, v11, s[14:15]
	v_cndmask_b32_e64 v2, v2, v12, s[14:15]
	v_cmp_ne_u32_e32 vcc, 0, v162
	s_nop 1
	v_mov_b32_e32 v10, vcc_lo
	v_mov_b32_e32 v11, vcc_hi
	v_cmp_ne_u32_e32 vcc, 0, v163
	v_cndmask_b32_e64 v2, v2, v10, s[16:17]
	v_cndmask_b32_e64 v8, v9, v11, s[16:17]
	v_mov_b32_e32 v9, vcc_hi
	v_mov_b32_e32 v10, vcc_lo
	v_cndmask_b32_e64 v9, v8, v9, s[18:19]
	v_cndmask_b32_e64 v8, v2, v10, s[18:19]
	s_mov_b64 s[2:3], exec
	s_mov_b64 exec, s[0:1]
	global_store_dwordx2 v[4:5], v[8:9], off
	s_mov_b64 exec, s[2:3]
	v_cmp_ne_u64_e32 vcc, 0, v[8:9]
	s_and_b64 s[20:21], s[0:1], vcc
	s_cmp_lg_u64 s[20:21], 0
	s_cselect_b32 s20, 128, 0
	s_or_b32 s76, s76, s20
	v_cmp_ne_u64_e32 vcc, -1, v[8:9]
	s_and_b64 s[20:21], s[0:1], vcc
	s_cmp_lg_u64 s[20:21], 0
	s_cselect_b32 s20, 128, 0
	s_or_b32 s77, s77, s20
	v_lshl_add_u64 v[4:5], v[4:5], 0, 8
	global_load_dword v212, v96, s[60:61] offset:3584 nt
	global_load_dword v213, v96, s[62:63] offset:3584 nt
	global_load_dword v214, v96, s[64:65] offset:3584 nt
	global_load_dword v215, v96, s[66:67] offset:3584 nt
	global_load_dword v216, v96, s[68:69] offset:3584 nt
	global_load_dword v217, v96, s[70:71] offset:3584 nt
	global_load_dword v218, v96, s[72:73] offset:3584 nt
	global_load_dword v219, v96, s[74:75] offset:3584 nt
	s_waitcnt vmcnt(54)
	v_cmp_ne_u32_e32 vcc, 0, v164
	s_nop 1
	v_mov_b32_e32 v2, vcc_lo
	v_mov_b32_e32 v9, vcc_hi
	v_cmp_ne_u32_e32 vcc, 0, v165
	v_cndmask_b32_e64 v2, 0, v2, s[22:23]
	v_cndmask_b32_e64 v9, 0, v9, s[22:23]
	v_mov_b32_e32 v11, vcc_hi
	v_mov_b32_e32 v14, vcc_lo
	v_cndmask_b32_e64 v9, v9, v11, s[6:7]
	v_cndmask_b32_e64 v2, v2, v14, s[6:7]
	v_cmp_ne_u32_e32 vcc, 0, v166
	s_nop 1
	v_mov_b32_e32 v11, vcc_lo
	v_mov_b32_e32 v14, vcc_hi
	v_cmp_ne_u32_e32 vcc, 0, v167
	v_cndmask_b32_e64 v2, v2, v11, s[8:9]
	v_cndmask_b32_e64 v9, v9, v14, s[8:9]
	v_mov_b32_e32 v11, vcc_hi
	v_mov_b32_e32 v14, vcc_lo
	v_cmp_ne_u32_e32 vcc, 0, v168
	v_cndmask_b32_e64 v9, v9, v11, s[10:11]
	v_cndmask_b32_e64 v2, v2, v14, s[10:11]
	v_mov_b32_e32 v11, vcc_lo
	v_mov_b32_e32 v12, vcc_hi
	v_cmp_ne_u32_e32 vcc, 0, v169
	v_cndmask_b32_e64 v2, v2, v11, s[12:13]
	v_cndmask_b32_e64 v9, v9, v12, s[12:13]
	v_mov_b32_e32 v11, vcc_hi
	v_mov_b32_e32 v12, vcc_lo
	v_cndmask_b32_e64 v9, v9, v11, s[14:15]
	v_cndmask_b32_e64 v2, v2, v12, s[14:15]
	v_cmp_ne_u32_e32 vcc, 0, v170
	s_nop 1
	v_mov_b32_e32 v10, vcc_lo
	v_mov_b32_e32 v11, vcc_hi
	v_cmp_ne_u32_e32 vcc, 0, v171
	v_cndmask_b32_e64 v2, v2, v10, s[16:17]
	v_cndmask_b32_e64 v8, v9, v11, s[16:17]
	v_mov_b32_e32 v9, vcc_hi
	v_mov_b32_e32 v10, vcc_lo
	v_cndmask_b32_e64 v9, v8, v9, s[18:19]
	v_cndmask_b32_e64 v8, v2, v10, s[18:19]
	s_mov_b64 s[2:3], exec
	s_mov_b64 exec, s[0:1]
	global_store_dwordx2 v[4:5], v[8:9], off
	s_mov_b64 exec, s[2:3]
	v_cmp_ne_u64_e32 vcc, 0, v[8:9]
	s_and_b64 s[20:21], s[0:1], vcc
	s_cmp_lg_u64 s[20:21], 0
	s_cselect_b32 s20, 256, 0
	s_or_b32 s76, s76, s20
	v_cmp_ne_u64_e32 vcc, -1, v[8:9]
	s_and_b64 s[20:21], s[0:1], vcc
	s_cmp_lg_u64 s[20:21], 0
	s_cselect_b32 s20, 256, 0
	s_or_b32 s77, s77, s20
	v_lshl_add_u64 v[4:5], v[4:5], 0, 8
	global_load_dword v220, v96, s[60:61] offset:3840 nt
	global_load_dword v221, v96, s[62:63] offset:3840 nt
	global_load_dword v222, v96, s[64:65] offset:3840 nt
	global_load_dword v223, v96, s[66:67] offset:3840 nt
	global_load_dword v224, v96, s[68:69] offset:3840 nt
	global_load_dword v225, v96, s[70:71] offset:3840 nt
	global_load_dword v226, v96, s[72:73] offset:3840 nt
	global_load_dword v227, v96, s[74:75] offset:3840 nt
	s_waitcnt vmcnt(54)
	v_cmp_ne_u32_e32 vcc, 0, v172
	s_nop 1
	v_mov_b32_e32 v2, vcc_lo
	v_mov_b32_e32 v9, vcc_hi
	v_cmp_ne_u32_e32 vcc, 0, v173
	v_cndmask_b32_e64 v2, 0, v2, s[22:23]
	v_cndmask_b32_e64 v9, 0, v9, s[22:23]
	v_mov_b32_e32 v11, vcc_hi
	v_mov_b32_e32 v14, vcc_lo
	v_cndmask_b32_e64 v9, v9, v11, s[6:7]
	v_cndmask_b32_e64 v2, v2, v14, s[6:7]
	v_cmp_ne_u32_e32 vcc, 0, v174
	s_nop 1
	v_mov_b32_e32 v11, vcc_lo
	v_mov_b32_e32 v14, vcc_hi
	v_cmp_ne_u32_e32 vcc, 0, v175
	v_cndmask_b32_e64 v2, v2, v11, s[8:9]
	v_cndmask_b32_e64 v9, v9, v14, s[8:9]
	v_mov_b32_e32 v11, vcc_hi
	v_mov_b32_e32 v14, vcc_lo
	v_cmp_ne_u32_e32 vcc, 0, v176
	v_cndmask_b32_e64 v9, v9, v11, s[10:11]
	v_cndmask_b32_e64 v2, v2, v14, s[10:11]
	v_mov_b32_e32 v11, vcc_lo
	v_mov_b32_e32 v12, vcc_hi
	v_cmp_ne_u32_e32 vcc, 0, v177
	v_cndmask_b32_e64 v2, v2, v11, s[12:13]
	v_cndmask_b32_e64 v9, v9, v12, s[12:13]
	v_mov_b32_e32 v11, vcc_hi
	v_mov_b32_e32 v12, vcc_lo
	v_cndmask_b32_e64 v9, v9, v11, s[14:15]
	v_cndmask_b32_e64 v2, v2, v12, s[14:15]
	v_cmp_ne_u32_e32 vcc, 0, v178
	s_nop 1
	v_mov_b32_e32 v10, vcc_lo
	v_mov_b32_e32 v11, vcc_hi
	v_cmp_ne_u32_e32 vcc, 0, v179
	v_cndmask_b32_e64 v2, v2, v10, s[16:17]
	v_cndmask_b32_e64 v8, v9, v11, s[16:17]
	v_mov_b32_e32 v9, vcc_hi
	v_mov_b32_e32 v10, vcc_lo
	v_cndmask_b32_e64 v9, v8, v9, s[18:19]
	v_cndmask_b32_e64 v8, v2, v10, s[18:19]
	s_mov_b64 s[2:3], exec
	s_mov_b64 exec, s[0:1]
	global_store_dwordx2 v[4:5], v[8:9], off
	s_mov_b64 exec, s[2:3]
	v_cmp_ne_u64_e32 vcc, 0, v[8:9]
	s_and_b64 s[20:21], s[0:1], vcc
	s_cmp_lg_u64 s[20:21], 0
	s_cselect_b32 s20, 512, 0
	s_or_b32 s76, s76, s20
	v_cmp_ne_u64_e32 vcc, -1, v[8:9]
	s_and_b64 s[20:21], s[0:1], vcc
	s_cmp_lg_u64 s[20:21], 0
	s_cselect_b32 s20, 512, 0
	s_or_b32 s77, s77, s20
	v_lshl_add_u64 v[4:5], v[4:5], 0, 8
	s_waitcnt vmcnt(46)
	v_cmp_ne_u32_e32 vcc, 0, v180
	s_nop 1
	v_mov_b32_e32 v2, vcc_lo
	v_mov_b32_e32 v9, vcc_hi
	v_cmp_ne_u32_e32 vcc, 0, v181
	v_cndmask_b32_e64 v2, 0, v2, s[22:23]
	v_cndmask_b32_e64 v9, 0, v9, s[22:23]
	v_mov_b32_e32 v11, vcc_hi
	v_mov_b32_e32 v14, vcc_lo
	v_cndmask_b32_e64 v9, v9, v11, s[6:7]
	v_cndmask_b32_e64 v2, v2, v14, s[6:7]
	v_cmp_ne_u32_e32 vcc, 0, v182
	s_nop 1
	v_mov_b32_e32 v11, vcc_lo
	v_mov_b32_e32 v14, vcc_hi
	v_cmp_ne_u32_e32 vcc, 0, v183
	v_cndmask_b32_e64 v2, v2, v11, s[8:9]
	v_cndmask_b32_e64 v9, v9, v14, s[8:9]
	v_mov_b32_e32 v11, vcc_hi
	v_mov_b32_e32 v14, vcc_lo
	v_cmp_ne_u32_e32 vcc, 0, v184
	v_cndmask_b32_e64 v9, v9, v11, s[10:11]
	v_cndmask_b32_e64 v2, v2, v14, s[10:11]
	v_mov_b32_e32 v11, vcc_lo
	v_mov_b32_e32 v12, vcc_hi
	v_cmp_ne_u32_e32 vcc, 0, v185
	v_cndmask_b32_e64 v2, v2, v11, s[12:13]
	v_cndmask_b32_e64 v9, v9, v12, s[12:13]
	v_mov_b32_e32 v11, vcc_hi
	v_mov_b32_e32 v12, vcc_lo
	v_cndmask_b32_e64 v9, v9, v11, s[14:15]
	v_cndmask_b32_e64 v2, v2, v12, s[14:15]
	v_cmp_ne_u32_e32 vcc, 0, v186
	s_nop 1
	v_mov_b32_e32 v10, vcc_lo
	v_mov_b32_e32 v11, vcc_hi
	v_cmp_ne_u32_e32 vcc, 0, v187
	v_cndmask_b32_e64 v2, v2, v10, s[16:17]
	v_cndmask_b32_e64 v8, v9, v11, s[16:17]
	v_mov_b32_e32 v9, vcc_hi
	v_mov_b32_e32 v10, vcc_lo
	v_cndmask_b32_e64 v9, v8, v9, s[18:19]
	v_cndmask_b32_e64 v8, v2, v10, s[18:19]
	s_mov_b64 s[2:3], exec
	s_mov_b64 exec, s[0:1]
	global_store_dwordx2 v[4:5], v[8:9], off
	s_mov_b64 exec, s[2:3]
	v_cmp_ne_u64_e32 vcc, 0, v[8:9]
	s_and_b64 s[20:21], s[0:1], vcc
	s_cmp_lg_u64 s[20:21], 0
	s_cselect_b32 s20, 1024, 0
	s_or_b32 s76, s76, s20
	v_cmp_ne_u64_e32 vcc, -1, v[8:9]
	s_and_b64 s[20:21], s[0:1], vcc
	s_cmp_lg_u64 s[20:21], 0
	s_cselect_b32 s20, 1024, 0
	s_or_b32 s77, s77, s20
	v_lshl_add_u64 v[4:5], v[4:5], 0, 8
	s_waitcnt vmcnt(38)
	v_cmp_ne_u32_e32 vcc, 0, v188
	s_nop 1
	v_mov_b32_e32 v2, vcc_lo
	v_mov_b32_e32 v9, vcc_hi
	v_cmp_ne_u32_e32 vcc, 0, v189
	v_cndmask_b32_e64 v2, 0, v2, s[22:23]
	v_cndmask_b32_e64 v9, 0, v9, s[22:23]
	v_mov_b32_e32 v11, vcc_hi
	v_mov_b32_e32 v14, vcc_lo
	v_cndmask_b32_e64 v9, v9, v11, s[6:7]
	v_cndmask_b32_e64 v2, v2, v14, s[6:7]
	v_cmp_ne_u32_e32 vcc, 0, v190
	s_nop 1
	v_mov_b32_e32 v11, vcc_lo
	v_mov_b32_e32 v14, vcc_hi
	v_cmp_ne_u32_e32 vcc, 0, v191
	v_cndmask_b32_e64 v2, v2, v11, s[8:9]
	v_cndmask_b32_e64 v9, v9, v14, s[8:9]
	v_mov_b32_e32 v11, vcc_hi
	v_mov_b32_e32 v14, vcc_lo
	v_cmp_ne_u32_e32 vcc, 0, v192
	v_cndmask_b32_e64 v9, v9, v11, s[10:11]
	v_cndmask_b32_e64 v2, v2, v14, s[10:11]
	v_mov_b32_e32 v11, vcc_lo
	v_mov_b32_e32 v12, vcc_hi
	v_cmp_ne_u32_e32 vcc, 0, v193
	v_cndmask_b32_e64 v2, v2, v11, s[12:13]
	v_cndmask_b32_e64 v9, v9, v12, s[12:13]
	v_mov_b32_e32 v11, vcc_hi
	v_mov_b32_e32 v12, vcc_lo
	v_cndmask_b32_e64 v9, v9, v11, s[14:15]
	v_cndmask_b32_e64 v2, v2, v12, s[14:15]
	v_cmp_ne_u32_e32 vcc, 0, v194
	s_nop 1
	v_mov_b32_e32 v10, vcc_lo
	v_mov_b32_e32 v11, vcc_hi
	v_cmp_ne_u32_e32 vcc, 0, v195
	v_cndmask_b32_e64 v2, v2, v10, s[16:17]
	v_cndmask_b32_e64 v8, v9, v11, s[16:17]
	v_mov_b32_e32 v9, vcc_hi
	v_mov_b32_e32 v10, vcc_lo
	v_cndmask_b32_e64 v9, v8, v9, s[18:19]
	v_cndmask_b32_e64 v8, v2, v10, s[18:19]
	s_mov_b64 s[2:3], exec
	s_mov_b64 exec, s[0:1]
	global_store_dwordx2 v[4:5], v[8:9], off
	s_mov_b64 exec, s[2:3]
	v_cmp_ne_u64_e32 vcc, 0, v[8:9]
	s_and_b64 s[20:21], s[0:1], vcc
	s_cmp_lg_u64 s[20:21], 0
	s_cselect_b32 s20, 2048, 0
	s_or_b32 s76, s76, s20
	v_cmp_ne_u64_e32 vcc, -1, v[8:9]
	s_and_b64 s[20:21], s[0:1], vcc
	s_cmp_lg_u64 s[20:21], 0
	s_cselect_b32 s20, 2048, 0
	s_or_b32 s77, s77, s20
	v_lshl_add_u64 v[4:5], v[4:5], 0, 8
	s_waitcnt vmcnt(30)
	v_cmp_ne_u32_e32 vcc, 0, v196
	s_nop 1
	v_mov_b32_e32 v2, vcc_lo
	v_mov_b32_e32 v9, vcc_hi
	v_cmp_ne_u32_e32 vcc, 0, v197
	v_cndmask_b32_e64 v2, 0, v2, s[22:23]
	v_cndmask_b32_e64 v9, 0, v9, s[22:23]
	v_mov_b32_e32 v11, vcc_hi
	v_mov_b32_e32 v14, vcc_lo
	v_cndmask_b32_e64 v9, v9, v11, s[6:7]
	v_cndmask_b32_e64 v2, v2, v14, s[6:7]
	v_cmp_ne_u32_e32 vcc, 0, v198
	s_nop 1
	v_mov_b32_e32 v11, vcc_lo
	v_mov_b32_e32 v14, vcc_hi
	v_cmp_ne_u32_e32 vcc, 0, v199
	v_cndmask_b32_e64 v2, v2, v11, s[8:9]
	v_cndmask_b32_e64 v9, v9, v14, s[8:9]
	v_mov_b32_e32 v11, vcc_hi
	v_mov_b32_e32 v14, vcc_lo
	v_cmp_ne_u32_e32 vcc, 0, v200
	v_cndmask_b32_e64 v9, v9, v11, s[10:11]
	v_cndmask_b32_e64 v2, v2, v14, s[10:11]
	v_mov_b32_e32 v11, vcc_lo
	v_mov_b32_e32 v12, vcc_hi
	v_cmp_ne_u32_e32 vcc, 0, v201
	v_cndmask_b32_e64 v2, v2, v11, s[12:13]
	v_cndmask_b32_e64 v9, v9, v12, s[12:13]
	v_mov_b32_e32 v11, vcc_hi
	v_mov_b32_e32 v12, vcc_lo
	v_cndmask_b32_e64 v9, v9, v11, s[14:15]
	v_cndmask_b32_e64 v2, v2, v12, s[14:15]
	v_cmp_ne_u32_e32 vcc, 0, v202
	s_nop 1
	v_mov_b32_e32 v10, vcc_lo
	v_mov_b32_e32 v11, vcc_hi
	v_cmp_ne_u32_e32 vcc, 0, v203
	v_cndmask_b32_e64 v2, v2, v10, s[16:17]
	v_cndmask_b32_e64 v8, v9, v11, s[16:17]
	v_mov_b32_e32 v9, vcc_hi
	v_mov_b32_e32 v10, vcc_lo
	v_cndmask_b32_e64 v9, v8, v9, s[18:19]
	v_cndmask_b32_e64 v8, v2, v10, s[18:19]
	s_mov_b64 s[2:3], exec
	s_mov_b64 exec, s[0:1]
	global_store_dwordx2 v[4:5], v[8:9], off
	s_mov_b64 exec, s[2:3]
	v_cmp_ne_u64_e32 vcc, 0, v[8:9]
	s_and_b64 s[20:21], s[0:1], vcc
	s_cmp_lg_u64 s[20:21], 0
	s_cselect_b32 s20, 4096, 0
	s_or_b32 s76, s76, s20
	v_cmp_ne_u64_e32 vcc, -1, v[8:9]
	s_and_b64 s[20:21], s[0:1], vcc
	s_cmp_lg_u64 s[20:21], 0
	s_cselect_b32 s20, 4096, 0
	s_or_b32 s77, s77, s20
	v_lshl_add_u64 v[4:5], v[4:5], 0, 8
	s_waitcnt vmcnt(22)
	v_cmp_ne_u32_e32 vcc, 0, v204
	s_nop 1
	v_mov_b32_e32 v2, vcc_lo
	v_mov_b32_e32 v9, vcc_hi
	v_cmp_ne_u32_e32 vcc, 0, v205
	v_cndmask_b32_e64 v2, 0, v2, s[22:23]
	v_cndmask_b32_e64 v9, 0, v9, s[22:23]
	v_mov_b32_e32 v11, vcc_hi
	v_mov_b32_e32 v14, vcc_lo
	v_cndmask_b32_e64 v9, v9, v11, s[6:7]
	v_cndmask_b32_e64 v2, v2, v14, s[6:7]
	v_cmp_ne_u32_e32 vcc, 0, v206
	s_nop 1
	v_mov_b32_e32 v11, vcc_lo
	v_mov_b32_e32 v14, vcc_hi
	v_cmp_ne_u32_e32 vcc, 0, v207
	v_cndmask_b32_e64 v2, v2, v11, s[8:9]
	v_cndmask_b32_e64 v9, v9, v14, s[8:9]
	v_mov_b32_e32 v11, vcc_hi
	v_mov_b32_e32 v14, vcc_lo
	v_cmp_ne_u32_e32 vcc, 0, v208
	v_cndmask_b32_e64 v9, v9, v11, s[10:11]
	v_cndmask_b32_e64 v2, v2, v14, s[10:11]
	v_mov_b32_e32 v11, vcc_lo
	v_mov_b32_e32 v12, vcc_hi
	v_cmp_ne_u32_e32 vcc, 0, v209
	v_cndmask_b32_e64 v2, v2, v11, s[12:13]
	v_cndmask_b32_e64 v9, v9, v12, s[12:13]
	v_mov_b32_e32 v11, vcc_hi
	v_mov_b32_e32 v12, vcc_lo
	v_cndmask_b32_e64 v9, v9, v11, s[14:15]
	v_cndmask_b32_e64 v2, v2, v12, s[14:15]
	v_cmp_ne_u32_e32 vcc, 0, v210
	s_nop 1
	v_mov_b32_e32 v10, vcc_lo
	v_mov_b32_e32 v11, vcc_hi
	v_cmp_ne_u32_e32 vcc, 0, v211
	v_cndmask_b32_e64 v2, v2, v10, s[16:17]
	v_cndmask_b32_e64 v8, v9, v11, s[16:17]
	v_mov_b32_e32 v9, vcc_hi
	v_mov_b32_e32 v10, vcc_lo
	v_cndmask_b32_e64 v9, v8, v9, s[18:19]
	v_cndmask_b32_e64 v8, v2, v10, s[18:19]
	s_mov_b64 s[2:3], exec
	s_mov_b64 exec, s[0:1]
	global_store_dwordx2 v[4:5], v[8:9], off
	s_mov_b64 exec, s[2:3]
	v_cmp_ne_u64_e32 vcc, 0, v[8:9]
	s_and_b64 s[20:21], s[0:1], vcc
	s_cmp_lg_u64 s[20:21], 0
	s_cselect_b32 s20, 8192, 0
	s_or_b32 s76, s76, s20
	v_cmp_ne_u64_e32 vcc, -1, v[8:9]
	s_and_b64 s[20:21], s[0:1], vcc
	s_cmp_lg_u64 s[20:21], 0
	s_cselect_b32 s20, 8192, 0
	s_or_b32 s77, s77, s20
	v_lshl_add_u64 v[4:5], v[4:5], 0, 8
	s_waitcnt vmcnt(14)
	v_cmp_ne_u32_e32 vcc, 0, v212
	s_nop 1
	v_mov_b32_e32 v2, vcc_lo
	v_mov_b32_e32 v9, vcc_hi
	v_cmp_ne_u32_e32 vcc, 0, v213
	v_cndmask_b32_e64 v2, 0, v2, s[22:23]
	v_cndmask_b32_e64 v9, 0, v9, s[22:23]
	v_mov_b32_e32 v11, vcc_hi
	v_mov_b32_e32 v14, vcc_lo
	v_cndmask_b32_e64 v9, v9, v11, s[6:7]
	v_cndmask_b32_e64 v2, v2, v14, s[6:7]
	v_cmp_ne_u32_e32 vcc, 0, v214
	s_nop 1
	v_mov_b32_e32 v11, vcc_lo
	v_mov_b32_e32 v14, vcc_hi
	v_cmp_ne_u32_e32 vcc, 0, v215
	v_cndmask_b32_e64 v2, v2, v11, s[8:9]
	v_cndmask_b32_e64 v9, v9, v14, s[8:9]
	v_mov_b32_e32 v11, vcc_hi
	v_mov_b32_e32 v14, vcc_lo
	v_cmp_ne_u32_e32 vcc, 0, v216
	v_cndmask_b32_e64 v9, v9, v11, s[10:11]
	v_cndmask_b32_e64 v2, v2, v14, s[10:11]
	v_mov_b32_e32 v11, vcc_lo
	v_mov_b32_e32 v12, vcc_hi
	v_cmp_ne_u32_e32 vcc, 0, v217
	v_cndmask_b32_e64 v2, v2, v11, s[12:13]
	v_cndmask_b32_e64 v9, v9, v12, s[12:13]
	v_mov_b32_e32 v11, vcc_hi
	v_mov_b32_e32 v12, vcc_lo
	v_cndmask_b32_e64 v9, v9, v11, s[14:15]
	v_cndmask_b32_e64 v2, v2, v12, s[14:15]
	v_cmp_ne_u32_e32 vcc, 0, v218
	s_nop 1
	v_mov_b32_e32 v10, vcc_lo
	v_mov_b32_e32 v11, vcc_hi
	v_cmp_ne_u32_e32 vcc, 0, v219
	v_cndmask_b32_e64 v2, v2, v10, s[16:17]
	v_cndmask_b32_e64 v8, v9, v11, s[16:17]
	v_mov_b32_e32 v9, vcc_hi
	v_mov_b32_e32 v10, vcc_lo
	v_cndmask_b32_e64 v9, v8, v9, s[18:19]
	v_cndmask_b32_e64 v8, v2, v10, s[18:19]
	s_mov_b64 s[2:3], exec
	s_mov_b64 exec, s[0:1]
	global_store_dwordx2 v[4:5], v[8:9], off
	s_mov_b64 exec, s[2:3]
	v_cmp_ne_u64_e32 vcc, 0, v[8:9]
	s_and_b64 s[20:21], s[0:1], vcc
	s_cmp_lg_u64 s[20:21], 0
	s_cselect_b32 s20, 16384, 0
	s_or_b32 s76, s76, s20
	v_cmp_ne_u64_e32 vcc, -1, v[8:9]
	s_and_b64 s[20:21], s[0:1], vcc
	s_cmp_lg_u64 s[20:21], 0
	s_cselect_b32 s20, 16384, 0
	s_or_b32 s77, s77, s20
	v_lshl_add_u64 v[4:5], v[4:5], 0, 8
	s_waitcnt vmcnt(6)
	v_cmp_ne_u32_e32 vcc, 0, v220
	s_nop 1
	v_mov_b32_e32 v2, vcc_lo
	v_mov_b32_e32 v9, vcc_hi
	v_cmp_ne_u32_e32 vcc, 0, v221
	v_cndmask_b32_e64 v2, 0, v2, s[22:23]
	v_cndmask_b32_e64 v9, 0, v9, s[22:23]
	v_mov_b32_e32 v11, vcc_hi
	v_mov_b32_e32 v14, vcc_lo
	v_cndmask_b32_e64 v9, v9, v11, s[6:7]
	v_cndmask_b32_e64 v2, v2, v14, s[6:7]
	v_cmp_ne_u32_e32 vcc, 0, v222
	s_nop 1
	v_mov_b32_e32 v11, vcc_lo
	v_mov_b32_e32 v14, vcc_hi
	v_cmp_ne_u32_e32 vcc, 0, v223
	v_cndmask_b32_e64 v2, v2, v11, s[8:9]
	v_cndmask_b32_e64 v9, v9, v14, s[8:9]
	v_mov_b32_e32 v11, vcc_hi
	v_mov_b32_e32 v14, vcc_lo
	v_cmp_ne_u32_e32 vcc, 0, v224
	v_cndmask_b32_e64 v9, v9, v11, s[10:11]
	v_cndmask_b32_e64 v2, v2, v14, s[10:11]
	v_mov_b32_e32 v11, vcc_lo
	v_mov_b32_e32 v12, vcc_hi
	v_cmp_ne_u32_e32 vcc, 0, v225
	v_cndmask_b32_e64 v2, v2, v11, s[12:13]
	v_cndmask_b32_e64 v9, v9, v12, s[12:13]
	v_mov_b32_e32 v11, vcc_hi
	v_mov_b32_e32 v12, vcc_lo
	v_cndmask_b32_e64 v9, v9, v11, s[14:15]
	v_cndmask_b32_e64 v2, v2, v12, s[14:15]
	v_cmp_ne_u32_e32 vcc, 0, v226
	s_nop 1
	v_mov_b32_e32 v10, vcc_lo
	v_mov_b32_e32 v11, vcc_hi
	v_cmp_ne_u32_e32 vcc, 0, v227
	v_cndmask_b32_e64 v2, v2, v10, s[16:17]
	v_cndmask_b32_e64 v8, v9, v11, s[16:17]
	v_mov_b32_e32 v9, vcc_hi
	v_mov_b32_e32 v10, vcc_lo
	v_cndmask_b32_e64 v9, v8, v9, s[18:19]
	v_cndmask_b32_e64 v8, v2, v10, s[18:19]
	s_mov_b64 s[2:3], exec
	s_mov_b64 exec, s[0:1]
	global_store_dwordx2 v[4:5], v[8:9], off
	s_mov_b64 exec, s[2:3]
	v_cmp_ne_u64_e32 vcc, 0, v[8:9]
	s_and_b64 s[20:21], s[0:1], vcc
	s_cmp_lg_u64 s[20:21], 0
	s_cselect_b32 s20, 32768, 0
	s_or_b32 s76, s76, s20
	v_cmp_ne_u64_e32 vcc, -1, v[8:9]
	s_and_b64 s[20:21], s[0:1], vcc
	s_cmp_lg_u64 s[20:21], 0
	s_cselect_b32 s20, 32768, 0
	s_or_b32 s77, s77, s20
	v_lshl_add_u64 v[4:5], v[4:5], 0, 8
	v_mov_b32_e32 v2, s76
	v_mov_b32_e32 v8, s77
	s_mov_b64 s[2:3], exec
	s_mov_b64 exec, s[22:23]
	ds_write2_b32 v1, v2, v8 offset1:8
	s_mov_b64 exec, s[2:3]
	s_waitcnt lgkmcnt(0)
	s_barrier
	ds_read_b128 v[8:11], v3
	ds_read_b128 v[12:15], v3 offset:16
	ds_read_b128 v[16:19], v3 offset:32
	ds_read_b128 v[20:23], v3 offset:48
	s_waitcnt lgkmcnt(0)
	v_or_b32_e32 v8, v8, v9
	v_or3_b32 v8, v8, v10, v11
	v_or3_b32 v8, v8, v12, v13
	v_or3_b32 v8, v8, v14, v15
	v_or_b32_e32 v16, v16, v17
	v_or3_b32 v16, v16, v18, v19
	v_or3_b32 v16, v16, v20, v21
	v_or3_b32 v16, v16, v22, v23
	v_and_b32_e32 v2, 15, v0
	v_lshrrev_b32_e32 v8, v2, v8
	v_and_b32_e32 v8, 1, v8
	v_lshrrev_b32_e32 v16, v2, v16
	v_and_b32_e32 v16, 1, v16
	v_lshl_or_b32 v8, v16, 1, v8
	v_lshlrev_b32_e32 v2, 2, v2
	v_cmp_gt_u32_e32 vcc, 16, v0
	s_and_saveexec_b64 s[2:3], vcc
	global_store_dword v2, v8, s[26:27]
	s_mov_b64 exec, s[2:3]
	v_mov_b32_e32 v230, v0
	s_mov_b32 s79, 0
